# v29: v26 + routing sigmoids (expf + IEEE divide, 16 per token, serial in wave 0) computed once per thread in the 256-thread logit-reduction stage and passed through LDS (identical instruction sequence
# speedup vs baseline: 1.0097x; 1.0097x over previous
.Lpf_skip_0:
	v_lshlrev_b32_e32 v90, 16, v88
	v_and_b32_e32 v91, 0xffff0000, v88
	v_sub_f32_e32 v90, v86, v90
	v_sub_f32_e32 v91, v87, v91
	v_cvt_pk_bf16_f32 v89, v84, v85
	v_cvt_pk_bf16_f32 v90, v90, v91
	v_lshlrev_b32_e32 v128, 4, v128
	v_lshlrev_b32_e32 v91, 16, v89
	v_sub_f32_e32 v91, v84, v91
	v_and_b32_e32 v129, 0xffff0000, v89
	v_add3_u32 v128, s46, v128, v228
	v_sub_f32_e32 v129, v85, v129
	v_cvt_pk_bf16_f32 v91, v91, v129
	ds_write_b64 v128, v[88:89]
	v_add_u32_e32 v88, 0x10000, v128
	ds_write_b64 v88, v[90:91]
	v_mov_b32_e32 v90, 0
	v_cvt_pk_fp8_f32 v90, v154, v155
	v_mov_b32_e32 v91, 0
	v_cvt_pk_fp8_f32 v91, v174, v175
	v_lshl_add_u64 v[88:89], s[6:7], 0, v[78:79]
	v_cvt_pk_fp8_f32 v90, v152, v153 op_sel:[0,0,1]
	v_mov_b32_e32 v128, 0
	v_cvt_pk_fp8_f32 v91, v170, v171 op_sel:[0,0,1]
	v_cvt_pk_fp8_f32 v128, v186, v187
	global_store_dword v[88:89], v90, off
	v_lshl_add_u64 v[88:89], s[6:7], 0, v[76:77]
	v_mov_b32_e32 v90, 0
	global_store_dword v[88:89], v91, off
	v_cvt_pk_fp8_f32 v90, v158, v159
	v_mov_b32_e32 v91, 0
	v_cvt_pk_fp8_f32 v91, v178, v179
	v_cvt_pk_fp8_f32 v128, v184, v185 op_sel:[0,0,1]
	v_cvt_pk_fp8_f32 v90, v156, v157 op_sel:[0,0,1]
	v_lshl_add_u64 v[88:89], s[6:7], 0, v[74:75]
	v_cvt_pk_fp8_f32 v91, v176, v177 op_sel:[0,0,1]
	global_store_dword v[88:89], v128, off
	v_lshl_add_u64 v[88:89], s[6:7], 0, v[72:73]
	v_mov_b32_e32 v128, 0
	global_store_dword v[88:89], v90, off
	v_lshl_add_u64 v[88:89], s[6:7], 0, v[70:71]
	v_cvt_pk_fp8_f32 v128, v134, v135
	global_store_dword v[88:89], v91, off
	v_mov_b32_e32 v88, 0
	v_cvt_pk_fp8_f32 v88, v240, v241
	v_mov_b32_e32 v89, 0
	v_cvt_pk_fp8_f32 v89, v80, v81
	v_cvt_pk_fp8_f32 v128, v130, v131 op_sel:[0,0,1]
	v_cvt_pk_fp8_f32 v88, v238, v239 op_sel:[0,0,1]
	v_lshl_add_u64 v[80:81], s[6:7], 0, v[68:69]
	v_cvt_pk_fp8_f32 v89, v82, v83 op_sel:[0,0,1]
	global_store_dword v[80:81], v128, off
	v_lshl_add_u64 v[80:81], s[6:7], 0, v[66:67]
	global_store_dword v[80:81], v88, off
	v_lshl_add_u64 v[80:81], s[6:7], 0, v[64:65]
	global_store_dword v[80:81], v89, off
	v_mov_b32_e32 v80, 0
	v_mov_b32_e32 v81, 0
	v_cvt_pk_fp8_f32 v80, v146, v147
	v_cvt_pk_fp8_f32 v81, v164, v165
	s_add_i32 s6, s1, s18
	s_ashr_i32 s7, s6, 31
	s_lshl_b64 s[6:7], s[6:7], 11
	v_cvt_pk_fp8_f32 v80, v136, v137 op_sel:[0,0,1]
	v_cvt_pk_fp8_f32 v81, v162, v163 op_sel:[0,0,1]
	s_add_u32 s6, s41, s6
	s_addc_u32 s7, s42, s7
	v_lshl_add_u64 v[78:79], s[6:7], 0, v[78:79]
	v_lshl_add_u64 v[76:77], s[6:7], 0, v[76:77]
	v_mov_b32_e32 v82, 0
	global_store_dword v[78:79], v80, off
	global_store_dword v[76:77], v81, off
	v_mov_b32_e32 v76, 0
	v_mov_b32_e32 v77, 0
	v_cvt_pk_fp8_f32 v82, v182, v183
	v_cvt_pk_fp8_f32 v76, v150, v151
	v_cvt_pk_fp8_f32 v77, v172, v173
	v_lshl_add_u64 v[74:75], s[6:7], 0, v[74:75]
	v_cvt_pk_fp8_f32 v82, v180, v181 op_sel:[0,0,1]
	v_cvt_pk_fp8_f32 v76, v148, v149 op_sel:[0,0,1]
	v_cvt_pk_fp8_f32 v77, v168, v169 op_sel:[0,0,1]
	v_lshl_add_u64 v[72:73], s[6:7], 0, v[72:73]
	v_lshl_add_u64 v[70:71], s[6:7], 0, v[70:71]
	global_store_dword v[74:75], v82, off
	v_mov_b32_e32 v74, 0
	global_store_dword v[72:73], v76, off
	global_store_dword v[70:71], v77, off
	v_mov_b32_e32 v70, 0
	v_mov_b32_e32 v71, 0
	v_cvt_pk_fp8_f32 v74, v94, v95
	v_cvt_pk_fp8_f32 v70, v140, v141
	v_cvt_pk_fp8_f32 v71, v86, v87
	v_lshl_add_u64 v[68:69], s[6:7], 0, v[68:69]
	v_cvt_pk_fp8_f32 v74, v92, v93 op_sel:[0,0,1]
	v_cvt_pk_fp8_f32 v70, v138, v139 op_sel:[0,0,1]
	v_cvt_pk_fp8_f32 v71, v84, v85 op_sel:[0,0,1]
	v_lshl_add_u64 v[66:67], s[6:7], 0, v[66:67]
	v_lshl_add_u64 v[64:65], s[6:7], 0, v[64:65]
	global_store_dword v[68:69], v74, off
	global_store_dword v[66:67], v70, off
	global_store_dword v[64:65], v71, off
	s_waitcnt lgkmcnt(0)
	s_barrier
	ds_read_b128 v[64:67], v190
	ds_read_b128 v[68:71], v191
	s_waitcnt lgkmcnt(1)
	v_mfma_f32_16x16x32_bf16 v[72:75], v[0:3], v[64:67], 0
	v_mov_b32_e32 v128, v167
	v_mfma_f32_16x16x32_bf16 v[64:67], v[4:7], v[64:67], v[72:75]
	s_waitcnt lgkmcnt(0)
	v_mfma_f32_16x16x32_bf16 v[64:67], v[0:3], v[68:71], v[64:67]
	ds_read_b128 v[68:71], v192
	s_nop 2
	ds_read_b128 v[72:75], v193
	s_waitcnt lgkmcnt(1)
	v_mfma_f32_16x16x32_bf16 v[64:67], v[8:11], v[68:71], v[64:67]
	v_mfma_f32_16x16x32_bf16 v[64:67], v[12:15], v[68:71], v[64:67]
	s_waitcnt lgkmcnt(0)
	v_mfma_f32_16x16x32_bf16 v[64:67], v[8:11], v[72:75], v[64:67]
	ds_read_b128 v[68:71], v194
	ds_read_b128 v[72:75], v195
	s_waitcnt lgkmcnt(1)
	v_mfma_f32_16x16x32_bf16 v[64:67], v[16:19], v[68:71], v[64:67]
	v_mfma_f32_16x16x32_bf16 v[64:67], v[20:23], v[68:71], v[64:67]
	s_waitcnt lgkmcnt(0)
	v_mfma_f32_16x16x32_bf16 v[64:67], v[16:19], v[72:75], v[64:67]
	ds_read_b128 v[68:71], v196
	ds_read_b128 v[72:75], v197
	s_waitcnt lgkmcnt(1)
	v_mfma_f32_16x16x32_bf16 v[64:67], v[24:27], v[68:71], v[64:67]
	v_mfma_f32_16x16x32_bf16 v[64:67], v[28:31], v[68:71], v[64:67]
	s_waitcnt lgkmcnt(0)
	v_mfma_f32_16x16x32_bf16 v[64:67], v[24:27], v[72:75], v[64:67]
	ds_read_b128 v[68:71], v198
	ds_read_b128 v[72:75], v199
	s_waitcnt lgkmcnt(1)
	v_mfma_f32_16x16x32_bf16 v[64:67], v[32:35], v[68:71], v[64:67]
	v_mfma_f32_16x16x32_bf16 v[64:67], v[36:39], v[68:71], v[64:67]
	s_waitcnt lgkmcnt(0)
	v_mfma_f32_16x16x32_bf16 v[64:67], v[32:35], v[72:75], v[64:67]
	ds_read_b128 v[68:71], v200
	ds_read_b128 v[72:75], v201
	s_waitcnt lgkmcnt(1)
	v_mfma_f32_16x16x32_bf16 v[64:67], v[40:43], v[68:71], v[64:67]
	v_mfma_f32_16x16x32_bf16 v[64:67], v[44:47], v[68:71], v[64:67]
	s_waitcnt lgkmcnt(0)
	v_mfma_f32_16x16x32_bf16 v[64:67], v[40:43], v[72:75], v[64:67]
	ds_read_b128 v[68:71], v202
	ds_read_b128 v[72:75], v203
	s_waitcnt lgkmcnt(1)
	v_mfma_f32_16x16x32_bf16 v[64:67], v[48:51], v[68:71], v[64:67]
	v_mfma_f32_16x16x32_bf16 v[64:67], v[52:55], v[68:71], v[64:67]
	s_waitcnt lgkmcnt(0)
	v_mfma_f32_16x16x32_bf16 v[64:67], v[48:51], v[72:75], v[64:67]
	ds_read_b128 v[68:71], v204
	ds_read_b128 v[72:75], v205
	s_waitcnt lgkmcnt(1)
	v_mfma_f32_16x16x32_bf16 v[64:67], v[56:59], v[68:71], v[64:67]
	v_mfma_f32_16x16x32_bf16 v[64:67], v[60:63], v[68:71], v[64:67]
	s_waitcnt lgkmcnt(0)
	v_mfma_f32_16x16x32_bf16 v[64:67], v[56:59], v[72:75], v[64:67]
	s_nop 7
	ds_write_b128 v208, v[64:67]
	s_waitcnt lgkmcnt(0)
	s_barrier
	s_nop 0
	v_cmp_gt_i32_e32 vcc, s48, v128
	s_and_saveexec_b64 s[6:7], vcc
	s_cbranch_execz .LBB0_1743
	v_lshl_add_u32 v72, v128, 2, 0
	v_add_u32_e32 v70, 0x22000, v72
	ds_read2st64_b32 v[64:65], v70 offset1:4
	ds_read2st64_b32 v[66:67], v70 offset0:8 offset1:12
	ds_read2st64_b32 v[68:69], v70 offset0:16 offset1:20
	ds_read2st64_b32 v[70:71], v70 offset0:24 offset1:28
	s_waitcnt lgkmcnt(3)
	v_add_f32_e32 v64, 0, v64
	v_add_f32_e32 v64, v64, v65
	s_waitcnt lgkmcnt(2)
	v_add_f32_e32 v64, v64, v66
	v_add_f32_e32 v64, v64, v67
	s_waitcnt lgkmcnt(1)
	v_add_f32_e32 v64, v64, v68
	v_add_f32_e32 v64, v64, v69
	s_waitcnt lgkmcnt(0)
	v_add_f32_e32 v64, v64, v70
	v_add_f32_e32 v64, v64, v71
	v_add_u32_e32 v65, 0x21000, v72
	ds_write_b32 v65, v64
	v_mul_f32_e32 v142, 0xbfb8aa3b, v64
	v_fma_f32 v143, v64, s50, -v142
	v_rndne_f32_e32 v144, v142
	v_fmac_f32_e32 v143, 0xb2a5705f, v64
	v_sub_f32_e32 v142, v142, v144
	v_add_f32_e32 v142, v142, v143
	v_cvt_i32_f32_e32 v145, v144
	v_exp_f32_e32 v146, v142
	v_cmp_nlt_f32_e32 vcc, s51, v64
	v_ldexp_f32 v145, v146, v145
	s_nop 0
	v_cndmask_b32_e32 v145, 0, v145, vcc
	v_cmp_ngt_f32_e32 vcc, s52, v64
	s_nop 1
	v_cndmask_b32_e32 v145, v211, v145, vcc
	v_add_f32_e32 v145, 1.0, v145
	v_div_scale_f32 v146, s[98:99], v145, v145, 1.0
	v_rcp_f32_e32 v147, v146
	v_div_scale_f32 v148, vcc, 1.0, v145, 1.0
	v_fma_f32 v149, -v146, v147, 1.0
	v_fmac_f32_e32 v147, v149, v147
	v_mul_f32_e32 v149, v148, v147
	v_fma_f32 v150, -v146, v149, v148
	v_fmac_f32_e32 v149, v150, v147
	v_fma_f32 v146, -v146, v149, v148
	v_div_fmas_f32 v146, v146, v147, v149
	v_div_fixup_f32 v146, v146, v145, 1.0
	ds_write_b32 v65, v146 offset:1024
.LBB0_1743:
	s_or_b64 exec, exec, s[6:7]
	v_cmp_gt_i32_e32 vcc, 16, v128
	s_waitcnt lgkmcnt(0)
	s_barrier
	s_and_saveexec_b64 s[28:29], vcc
	s_cbranch_execz .LBB0_1736
	global_load_dwordx4 v[88:91], v209, s[26:27]
	global_load_dwordx4 v[80:83], v209, s[26:27] offset:16
	global_load_dwordx4 v[64:67], v209, s[26:27] offset:48
	global_load_dwordx4 v[72:75], v209, s[26:27] offset:32
	v_lshl_add_u32 v68, v128, 6, 0
	v_add_u32_e32 v68, 0x21000, v68
	ds_read_b128 v[168:171], v68 offset:1024
	ds_read_b128 v[172:175], v68 offset:1040
	ds_read_b128 v[176:179], v68 offset:1056
	ds_read_b128 v[180:183], v68 offset:1072
	ds_read_b128 v[92:95], v68
	ds_read_b128 v[84:87], v68 offset:16
	s_waitcnt lgkmcnt(1)
	ds_read_b128 v[76:79], v68 offset:32
	ds_read_b128 v[68:71], v68 offset:48
	s_nop 1
	s_nop 1
	v_mov_b32_e32 v132, v168
	v_mov_b32_e32 v92, v169
	s_waitcnt vmcnt(3)
	v_add_f32_e32 v93, v88, v132
	v_add_f32_e32 v88, v89, v92
	v_max_f32_e32 v89, 0xf149f2ca, v93
	v_cmp_lt_f32_e64 s[8:9], s53, v93
	v_mov_b32_e32 v129, v88
	v_cmp_ngt_f32_e64 s[6:7], v88, v89
	v_mov_b32_e32 v130, v89
	s_and_saveexec_b64 s[10:11], s[6:7]
	s_cbranch_execz .LBB0_1748
	v_mov_b32_e32 v130, 0xf149f2ca
	v_cmp_gt_f32_e32 vcc, v88, v130
	s_and_saveexec_b64 s[12:13], vcc
	v_mov_b32_e32 v130, v88
	s_or_b64 exec, exec, s[12:13]
	v_mov_b32_e32 v129, v89
.LBB0_1748:
	s_or_b64 exec, exec, s[10:11]
	s_nop 0
	s_nop 1
	s_nop 0
	v_mov_b32_e32 v93, v170
	v_add_f32_e32 v90, v90, v93
	v_cmp_ngt_f32_e32 vcc, v90, v129
	v_mov_b32_e32 v133, v90
	s_and_saveexec_b64 s[10:11], vcc
	s_cbranch_execz .LBB0_1752
	v_cmp_gt_f32_e32 vcc, v90, v130
	s_and_saveexec_b64 s[12:13], vcc
	v_mov_b32_e32 v130, v90
	s_or_b64 exec, exec, s[12:13]
	v_mov_b32_e32 v133, v129
	v_mov_b32_e32 v129, v130
.LBB0_1752:
	s_or_b64 exec, exec, s[10:11]
	s_nop 0
	s_nop 1
	s_nop 0
	v_mov_b32_e32 v130, v171
	v_add_f32_e32 v131, v91, v130
	v_cmp_ngt_f32_e32 vcc, v131, v133
	v_mov_b32_e32 v134, v131
	s_and_saveexec_b64 s[10:11], vcc
	s_cbranch_execz .LBB0_1756
	v_cmp_gt_f32_e32 vcc, v131, v129
	s_and_saveexec_b64 s[12:13], vcc
	v_mov_b32_e32 v129, v131
	s_or_b64 exec, exec, s[12:13]
	v_mov_b32_e32 v134, v133
	v_mov_b32_e32 v133, v129
.LBB0_1756:
	s_or_b64 exec, exec, s[10:11]
	s_waitcnt lgkmcnt(2)
	v_mov_b32_e32 v91, v172
	s_waitcnt vmcnt(2)
	v_add_f32_e32 v84, v80, v91
	s_nop 0
	v_mov_b32_e32 v85, v173
	v_add_f32_e32 v80, v81, v85
	v_max_f32_e32 v95, 0xf149f2ca, v84
	v_cmp_ngt_f32_e32 vcc, v80, v95
	v_mov_b32_e32 v94, v80
	s_and_saveexec_b64 s[10:11], vcc
	s_cbranch_execz .LBB0_1760
	v_mov_b32_e32 v81, 0xf149f2ca
	v_cmp_gt_f32_e32 vcc, v80, v81
	s_and_saveexec_b64 s[12:13], vcc
	v_mov_b32_e32 v81, v80
	s_or_b64 exec, exec, s[12:13]
	v_mov_b32_e32 v94, v95
	v_mov_b32_e32 v95, v81
.LBB0_1760:
	s_or_b64 exec, exec, s[10:11]
	s_nop 0
	s_nop 1
	s_nop 0
	v_mov_b32_e32 v81, v174
	v_add_f32_e32 v86, v82, v81
	v_cmp_ngt_f32_e32 vcc, v86, v94
	v_mov_b32_e32 v135, v86
	s_and_saveexec_b64 s[10:11], vcc
	s_cbranch_execz .LBB0_1764
	v_cmp_gt_f32_e32 vcc, v86, v95
	s_and_saveexec_b64 s[12:13], vcc
	v_mov_b32_e32 v95, v86
	s_or_b64 exec, exec, s[12:13]
	v_mov_b32_e32 v135, v94
	v_mov_b32_e32 v94, v95
.LBB0_1764:
	s_or_b64 exec, exec, s[10:11]
	s_nop 0
	s_nop 1
	s_nop 0
	v_mov_b32_e32 v95, v175
	v_add_f32_e32 v129, v83, v95
	v_cmp_ngt_f32_e32 vcc, v129, v135
	v_mov_b32_e32 v136, v129
	s_and_saveexec_b64 s[10:11], vcc
	s_cbranch_execz .LBB0_1768
	v_cmp_gt_f32_e32 vcc, v129, v94
	s_and_saveexec_b64 s[12:13], vcc
	v_mov_b32_e32 v94, v129
	s_or_b64 exec, exec, s[12:13]
	v_mov_b32_e32 v136, v135
	v_mov_b32_e32 v135, v94
.LBB0_1768:
	s_or_b64 exec, exec, s[10:11]
	s_waitcnt lgkmcnt(1)
	v_mov_b32_e32 v83, v176
	s_waitcnt vmcnt(0)
	v_add_f32_e32 v76, v72, v83
	s_nop 0
	v_mov_b32_e32 v77, v177
	v_add_f32_e32 v72, v73, v77
	v_max_f32_e32 v87, 0xf149f2ca, v76
	v_cmp_ngt_f32_e32 vcc, v72, v87
	v_mov_b32_e32 v73, v72
	s_and_saveexec_b64 s[10:11], vcc
	s_cbranch_execz .LBB0_1772
	v_mov_b32_e32 v82, 0xf149f2ca
	v_cmp_gt_f32_e32 vcc, v72, v82
	s_and_saveexec_b64 s[12:13], vcc
	v_mov_b32_e32 v82, v72
	s_or_b64 exec, exec, s[12:13]
	v_mov_b32_e32 v73, v87
	v_mov_b32_e32 v87, v82
.LBB0_1772:
	s_or_b64 exec, exec, s[10:11]
	s_nop 0
	s_nop 1
	s_nop 0
	v_mov_b32_e32 v78, v178
	v_add_f32_e32 v82, v74, v78
	v_cmp_ngt_f32_e32 vcc, v82, v73
	v_mov_b32_e32 v137, v82
	s_and_saveexec_b64 s[10:11], vcc
	s_cbranch_execz .LBB0_1776
	v_cmp_gt_f32_e32 vcc, v82, v87
	s_and_saveexec_b64 s[12:13], vcc
	v_mov_b32_e32 v87, v82
	s_or_b64 exec, exec, s[12:13]
	v_mov_b32_e32 v137, v73
	v_mov_b32_e32 v73, v87
.LBB0_1776:
	s_or_b64 exec, exec, s[10:11]
	s_nop 0
	s_nop 1
	s_nop 0
	v_mov_b32_e32 v87, v179
	v_add_f32_e32 v94, v75, v87
	v_cmp_ngt_f32_e32 vcc, v94, v137
	v_mov_b32_e32 v138, v94
	s_and_saveexec_b64 s[10:11], vcc
	s_cbranch_execz .LBB0_1780
	v_cmp_gt_f32_e32 vcc, v94, v73
	s_and_saveexec_b64 s[12:13], vcc
	v_mov_b32_e32 v73, v94
	s_or_b64 exec, exec, s[12:13]
	v_mov_b32_e32 v138, v137
	v_mov_b32_e32 v137, v73
.LBB0_1780:
	s_or_b64 exec, exec, s[10:11]
	s_waitcnt lgkmcnt(0)
	v_mov_b32_e32 v79, v180
	v_add_f32_e32 v74, v64, v79
	s_nop 0
	s_nop 0
	v_mov_b32_e32 v75, v181
	v_add_f32_e32 v73, v65, v75
	v_max_f32_e32 v68, 0xf149f2ca, v74
	v_cmp_ngt_f32_e32 vcc, v73, v68
	v_mov_b32_e32 v64, v73
	s_and_saveexec_b64 s[10:11], vcc
	s_cbranch_execz .LBB0_1784
	v_mov_b32_e32 v65, 0xf149f2ca
	v_cmp_gt_f32_e32 vcc, v73, v65
	s_and_saveexec_b64 s[12:13], vcc
	v_mov_b32_e32 v65, v73
	s_or_b64 exec, exec, s[12:13]
	v_mov_b32_e32 v64, v68
	v_mov_b32_e32 v68, v65
.LBB0_1784:
	s_or_b64 exec, exec, s[10:11]
	s_nop 0
	s_nop 1
	s_nop 0
	v_mov_b32_e32 v70, v182
	v_add_f32_e32 v66, v66, v70
	v_cmp_ngt_f32_e32 vcc, v66, v64
	v_mov_b32_e32 v65, v66
	s_and_saveexec_b64 s[10:11], vcc
	s_cbranch_execz .LBB0_1788
	v_cmp_gt_f32_e32 vcc, v66, v68
	s_and_saveexec_b64 s[12:13], vcc
	v_mov_b32_e32 v68, v66
	s_or_b64 exec, exec, s[12:13]
	v_mov_b32_e32 v65, v64
	v_mov_b32_e32 v64, v68
.LBB0_1788:
	s_or_b64 exec, exec, s[10:11]
	s_nop 0
	s_nop 1
	s_nop 0
	v_mov_b32_e32 v71, v183
	v_add_f32_e32 v67, v67, v71
	v_cmp_ngt_f32_e32 vcc, v67, v65
	v_mov_b32_e32 v68, v67
	s_and_saveexec_b64 s[10:11], vcc
	s_cbranch_execz .LBB0_1792
	v_cmp_gt_f32_e32 vcc, v67, v64
	s_and_saveexec_b64 s[12:13], vcc
	v_mov_b32_e32 v64, v67
	s_or_b64 exec, exec, s[12:13]
	v_mov_b32_e32 v68, v65
	v_mov_b32_e32 v65, v64

.Lpf_skip_1:
	v_lshlrev_b32_e32 v90, 16, v88
	v_and_b32_e32 v91, 0xffff0000, v88
	v_sub_f32_e32 v90, v86, v90
	v_sub_f32_e32 v91, v87, v91
	v_cvt_pk_bf16_f32 v89, v84, v85
	v_cvt_pk_bf16_f32 v90, v90, v91
	v_lshlrev_b32_e32 v128, 4, v128
	v_lshlrev_b32_e32 v91, 16, v89
	v_sub_f32_e32 v91, v84, v91
	v_and_b32_e32 v129, 0xffff0000, v89
	v_add3_u32 v128, s46, v128, v228
	v_sub_f32_e32 v129, v85, v129
	v_cvt_pk_bf16_f32 v91, v91, v129
	ds_write_b64 v128, v[88:89]
	v_add_u32_e32 v88, 0x10000, v128
	ds_write_b64 v88, v[90:91]
	v_mov_b32_e32 v90, 0
	v_cvt_pk_fp8_f32 v90, v154, v155
	v_mov_b32_e32 v91, 0
	v_cvt_pk_fp8_f32 v91, v174, v175
	v_lshl_add_u64 v[88:89], s[6:7], 0, v[78:79]
	v_cvt_pk_fp8_f32 v90, v152, v153 op_sel:[0,0,1]
	v_mov_b32_e32 v128, 0
	v_cvt_pk_fp8_f32 v91, v170, v171 op_sel:[0,0,1]
	v_cvt_pk_fp8_f32 v128, v186, v187
	global_store_dword v[88:89], v90, off
	v_lshl_add_u64 v[88:89], s[6:7], 0, v[76:77]
	v_mov_b32_e32 v90, 0
	global_store_dword v[88:89], v91, off
	v_cvt_pk_fp8_f32 v90, v158, v159
	v_mov_b32_e32 v91, 0
	v_cvt_pk_fp8_f32 v91, v178, v179
	v_cvt_pk_fp8_f32 v128, v184, v185 op_sel:[0,0,1]
	v_cvt_pk_fp8_f32 v90, v156, v157 op_sel:[0,0,1]
	v_lshl_add_u64 v[88:89], s[6:7], 0, v[74:75]
	v_cvt_pk_fp8_f32 v91, v176, v177 op_sel:[0,0,1]
	global_store_dword v[88:89], v128, off
	v_lshl_add_u64 v[88:89], s[6:7], 0, v[72:73]
	v_mov_b32_e32 v128, 0
	global_store_dword v[88:89], v90, off
	v_lshl_add_u64 v[88:89], s[6:7], 0, v[70:71]
	v_cvt_pk_fp8_f32 v128, v134, v135
	global_store_dword v[88:89], v91, off
	v_mov_b32_e32 v88, 0
	v_cvt_pk_fp8_f32 v88, v144, v145
	v_mov_b32_e32 v89, 0
	v_cvt_pk_fp8_f32 v89, v80, v81
	v_cvt_pk_fp8_f32 v128, v130, v131 op_sel:[0,0,1]
	v_cvt_pk_fp8_f32 v88, v242, v243 op_sel:[0,0,1]
	v_lshl_add_u64 v[80:81], s[6:7], 0, v[68:69]
	v_cvt_pk_fp8_f32 v89, v82, v83 op_sel:[0,0,1]
	global_store_dword v[80:81], v128, off
	v_lshl_add_u64 v[80:81], s[6:7], 0, v[66:67]
	global_store_dword v[80:81], v88, off
	v_lshl_add_u64 v[80:81], s[6:7], 0, v[64:65]
	global_store_dword v[80:81], v89, off
	v_mov_b32_e32 v80, 0
	v_mov_b32_e32 v81, 0
	v_cvt_pk_fp8_f32 v80, v146, v147
	v_cvt_pk_fp8_f32 v81, v164, v165
	s_add_i32 s6, s1, s18
	s_ashr_i32 s7, s6, 31
	s_lshl_b64 s[6:7], s[6:7], 11
	v_cvt_pk_fp8_f32 v80, v142, v143 op_sel:[0,0,1]
	v_cvt_pk_fp8_f32 v81, v162, v163 op_sel:[0,0,1]
	s_add_u32 s6, s41, s6
	s_addc_u32 s7, s42, s7
	v_lshl_add_u64 v[78:79], s[6:7], 0, v[78:79]
	v_lshl_add_u64 v[76:77], s[6:7], 0, v[76:77]
	v_mov_b32_e32 v82, 0
	global_store_dword v[78:79], v80, off
	global_store_dword v[76:77], v81, off
	v_mov_b32_e32 v76, 0
	v_mov_b32_e32 v77, 0
	v_cvt_pk_fp8_f32 v82, v182, v183
	v_cvt_pk_fp8_f32 v76, v150, v151
	v_cvt_pk_fp8_f32 v77, v172, v173
	v_lshl_add_u64 v[74:75], s[6:7], 0, v[74:75]
	v_cvt_pk_fp8_f32 v82, v180, v181 op_sel:[0,0,1]
	v_cvt_pk_fp8_f32 v76, v148, v149 op_sel:[0,0,1]
	v_cvt_pk_fp8_f32 v77, v168, v169 op_sel:[0,0,1]
	v_lshl_add_u64 v[72:73], s[6:7], 0, v[72:73]
	v_lshl_add_u64 v[70:71], s[6:7], 0, v[70:71]
	global_store_dword v[74:75], v82, off
	v_mov_b32_e32 v74, 0
	global_store_dword v[72:73], v76, off
	global_store_dword v[70:71], v77, off
	v_mov_b32_e32 v70, 0
	v_mov_b32_e32 v71, 0
	v_cvt_pk_fp8_f32 v74, v94, v95
	v_cvt_pk_fp8_f32 v70, v138, v139
	v_cvt_pk_fp8_f32 v71, v86, v87
	v_lshl_add_u64 v[68:69], s[6:7], 0, v[68:69]
	v_cvt_pk_fp8_f32 v74, v92, v93 op_sel:[0,0,1]
	v_cvt_pk_fp8_f32 v70, v136, v137 op_sel:[0,0,1]
	v_cvt_pk_fp8_f32 v71, v84, v85 op_sel:[0,0,1]
	v_lshl_add_u64 v[66:67], s[6:7], 0, v[66:67]
	v_lshl_add_u64 v[64:65], s[6:7], 0, v[64:65]
	global_store_dword v[68:69], v74, off
	global_store_dword v[66:67], v70, off
	global_store_dword v[64:65], v71, off
	s_waitcnt lgkmcnt(0)
	s_barrier
	ds_read_b128 v[64:67], v190
	ds_read_b128 v[68:71], v191
	s_waitcnt lgkmcnt(1)
	v_mfma_f32_16x16x32_bf16 v[72:75], v[0:3], v[64:67], 0
	v_mov_b32_e32 v128, v167
	v_mfma_f32_16x16x32_bf16 v[64:67], v[4:7], v[64:67], v[72:75]
	s_waitcnt lgkmcnt(0)
	v_mfma_f32_16x16x32_bf16 v[64:67], v[0:3], v[68:71], v[64:67]
	ds_read_b128 v[68:71], v192
	s_nop 2
	ds_read_b128 v[72:75], v193
	s_waitcnt lgkmcnt(1)
	v_mfma_f32_16x16x32_bf16 v[64:67], v[8:11], v[68:71], v[64:67]
	v_mfma_f32_16x16x32_bf16 v[64:67], v[12:15], v[68:71], v[64:67]
	s_waitcnt lgkmcnt(0)
	v_mfma_f32_16x16x32_bf16 v[64:67], v[8:11], v[72:75], v[64:67]
	ds_read_b128 v[68:71], v194
	ds_read_b128 v[72:75], v195
	s_waitcnt lgkmcnt(1)
	v_mfma_f32_16x16x32_bf16 v[64:67], v[16:19], v[68:71], v[64:67]
	v_mfma_f32_16x16x32_bf16 v[64:67], v[20:23], v[68:71], v[64:67]
	s_waitcnt lgkmcnt(0)
	v_mfma_f32_16x16x32_bf16 v[64:67], v[16:19], v[72:75], v[64:67]
	ds_read_b128 v[68:71], v196
	ds_read_b128 v[72:75], v197
	s_waitcnt lgkmcnt(1)
	v_mfma_f32_16x16x32_bf16 v[64:67], v[24:27], v[68:71], v[64:67]
	v_mfma_f32_16x16x32_bf16 v[64:67], v[28:31], v[68:71], v[64:67]
	s_waitcnt lgkmcnt(0)
	v_mfma_f32_16x16x32_bf16 v[64:67], v[24:27], v[72:75], v[64:67]
	ds_read_b128 v[68:71], v198
	ds_read_b128 v[72:75], v199
	s_waitcnt lgkmcnt(1)
	v_mfma_f32_16x16x32_bf16 v[64:67], v[32:35], v[68:71], v[64:67]
	v_mfma_f32_16x16x32_bf16 v[64:67], v[36:39], v[68:71], v[64:67]
	s_waitcnt lgkmcnt(0)
	v_mfma_f32_16x16x32_bf16 v[64:67], v[32:35], v[72:75], v[64:67]
	ds_read_b128 v[68:71], v200
	ds_read_b128 v[72:75], v201
	s_waitcnt lgkmcnt(1)
	v_mfma_f32_16x16x32_bf16 v[64:67], v[40:43], v[68:71], v[64:67]
	v_mfma_f32_16x16x32_bf16 v[64:67], v[44:47], v[68:71], v[64:67]
	s_waitcnt lgkmcnt(0)
	v_mfma_f32_16x16x32_bf16 v[64:67], v[40:43], v[72:75], v[64:67]
	ds_read_b128 v[68:71], v202
	ds_read_b128 v[72:75], v203
	s_waitcnt lgkmcnt(1)
	v_mfma_f32_16x16x32_bf16 v[64:67], v[48:51], v[68:71], v[64:67]
	v_mfma_f32_16x16x32_bf16 v[64:67], v[52:55], v[68:71], v[64:67]
	s_waitcnt lgkmcnt(0)
	v_mfma_f32_16x16x32_bf16 v[64:67], v[48:51], v[72:75], v[64:67]
	ds_read_b128 v[68:71], v204
	ds_read_b128 v[72:75], v205
	s_waitcnt lgkmcnt(1)
	v_mfma_f32_16x16x32_bf16 v[64:67], v[56:59], v[68:71], v[64:67]
	v_mfma_f32_16x16x32_bf16 v[64:67], v[60:63], v[68:71], v[64:67]
	s_waitcnt lgkmcnt(0)
	v_mfma_f32_16x16x32_bf16 v[64:67], v[56:59], v[72:75], v[64:67]
	s_nop 7
	ds_write_b128 v208, v[64:67]
	s_waitcnt lgkmcnt(0)
	s_barrier
	s_nop 0
	v_cmp_gt_i32_e32 vcc, s48, v128
	s_and_saveexec_b64 s[6:7], vcc
	s_cbranch_execz .LBB0_5172
	v_lshl_add_u32 v72, v128, 2, 0
	v_add_u32_e32 v70, 0x22000, v72
	ds_read2st64_b32 v[64:65], v70 offset1:4
	ds_read2st64_b32 v[66:67], v70 offset0:8 offset1:12
	ds_read2st64_b32 v[68:69], v70 offset0:16 offset1:20
	ds_read2st64_b32 v[70:71], v70 offset0:24 offset1:28
	s_waitcnt lgkmcnt(3)
	v_add_f32_e32 v64, 0, v64
	v_add_f32_e32 v64, v64, v65
	s_waitcnt lgkmcnt(2)
	v_add_f32_e32 v64, v64, v66
	v_add_f32_e32 v64, v64, v67
	s_waitcnt lgkmcnt(1)
	v_add_f32_e32 v64, v64, v68
	v_add_f32_e32 v64, v64, v69
	s_waitcnt lgkmcnt(0)
	v_add_f32_e32 v64, v64, v70
	v_add_f32_e32 v64, v64, v71
	v_add_u32_e32 v65, 0x21000, v72
	ds_write_b32 v65, v64
	v_mul_f32_e32 v142, 0xbfb8aa3b, v64
	v_fma_f32 v143, v64, s50, -v142
	v_rndne_f32_e32 v144, v142
	v_fmac_f32_e32 v143, 0xb2a5705f, v64
	v_sub_f32_e32 v142, v142, v144
	v_add_f32_e32 v142, v142, v143
	v_cvt_i32_f32_e32 v145, v144
	v_exp_f32_e32 v146, v142
	v_cmp_nlt_f32_e32 vcc, s51, v64
	v_ldexp_f32 v145, v146, v145
	s_nop 0
	v_cndmask_b32_e32 v145, 0, v145, vcc
	v_cmp_ngt_f32_e32 vcc, s52, v64
	s_nop 1
	v_cndmask_b32_e32 v145, v211, v145, vcc
	v_add_f32_e32 v145, 1.0, v145
	v_div_scale_f32 v146, s[98:99], v145, v145, 1.0
	v_rcp_f32_e32 v147, v146
	v_div_scale_f32 v148, vcc, 1.0, v145, 1.0
	v_fma_f32 v149, -v146, v147, 1.0
	v_fmac_f32_e32 v147, v149, v147
	v_mul_f32_e32 v149, v148, v147
	v_fma_f32 v150, -v146, v149, v148
	v_fmac_f32_e32 v149, v150, v147
	v_fma_f32 v146, -v146, v149, v148
	v_div_fmas_f32 v146, v146, v147, v149
	v_div_fixup_f32 v146, v146, v145, 1.0
	ds_write_b32 v65, v146 offset:1024
.LBB0_5172:
	s_or_b64 exec, exec, s[6:7]
	v_cmp_gt_i32_e32 vcc, 16, v128
	s_waitcnt lgkmcnt(0)
	s_barrier
	s_and_saveexec_b64 s[28:29], vcc
	s_cbranch_execz .LBB0_5165
	global_load_dwordx4 v[88:91], v209, s[20:21]
	global_load_dwordx4 v[80:83], v209, s[20:21] offset:16
	global_load_dwordx4 v[64:67], v209, s[20:21] offset:48
	global_load_dwordx4 v[72:75], v209, s[20:21] offset:32
	v_lshl_add_u32 v68, v128, 6, 0
	v_add_u32_e32 v68, 0x21000, v68
	ds_read_b128 v[168:171], v68 offset:1024
	ds_read_b128 v[172:175], v68 offset:1040
	ds_read_b128 v[176:179], v68 offset:1056
	ds_read_b128 v[180:183], v68 offset:1072
	ds_read_b128 v[92:95], v68
	ds_read_b128 v[84:87], v68 offset:16
	s_waitcnt lgkmcnt(1)
	ds_read_b128 v[76:79], v68 offset:32
	ds_read_b128 v[68:71], v68 offset:48
	s_nop 1
	s_nop 1
	v_mov_b32_e32 v132, v168
	v_mov_b32_e32 v92, v169
	s_waitcnt vmcnt(3)
	v_add_f32_e32 v93, v88, v132
	v_add_f32_e32 v88, v89, v92
	v_max_f32_e32 v89, 0xf149f2ca, v93
	v_cmp_lt_f32_e64 s[8:9], s53, v93
	v_mov_b32_e32 v129, v88
	v_cmp_ngt_f32_e64 s[6:7], v88, v89
	v_mov_b32_e32 v130, v89
	s_and_saveexec_b64 s[10:11], s[6:7]
	s_cbranch_execz .LBB0_5177
	v_mov_b32_e32 v130, 0xf149f2ca
	v_cmp_gt_f32_e32 vcc, v88, v130
	s_and_saveexec_b64 s[12:13], vcc
	v_mov_b32_e32 v130, v88
	s_or_b64 exec, exec, s[12:13]
	v_mov_b32_e32 v129, v89
